# baseline (speedup 1.0000x reference)
.LBB1_4:
	v_add_u32_e32 v182, s19, v191
	v_add_u32_e32 v238, s19, v192
	ds_read_b128 v[178:181], v182 offset:32768
	ds_read_b128 v[194:197], v182 offset:34816
	ds_read_b128 v[198:201], v182 offset:36864
	ds_read_b128 v[202:205], v182 offset:38912
	ds_read_b128 v[206:209], v238
	ds_read_b128 v[210:213], v238 offset:2048
	ds_read_b128 v[214:217], v238 offset:4096
	ds_read_b128 v[218:221], v238 offset:6144
	ds_read_b128 v[222:225], v238 offset:8192
	ds_read_b128 v[226:229], v238 offset:10240
	ds_read_b128 v[230:233], v238 offset:12288
	ds_read_b128 v[234:237], v238 offset:14336
	s_min_u32 s21, s20, 29
	s_xor_b32 s19, s19, 0x10000
	v_add_u32_e32 v239, s19, v189
	s_waitcnt vmcnt(11)
	v_cvt_pk_bf16_f32 v13, v12, v13
	v_cvt_pk_bf16_f32 v12, v10, v11
	s_waitcnt vmcnt(10)
	v_cvt_pk_bf16_f32 v11, v20, v21
	v_cvt_pk_bf16_f32 v10, v18, v19
	ds_write2st64_b64 v239, v[12:13], v[10:11] offset1:8
	s_waitcnt vmcnt(9)
	v_cvt_pk_bf16_f32 v11, v24, v25
	v_cvt_pk_bf16_f32 v10, v22, v23
	s_waitcnt vmcnt(8)
	v_cvt_pk_bf16_f32 v13, v32, v33
	v_cvt_pk_bf16_f32 v12, v30, v31
	ds_write2st64_b64 v239, v[10:11], v[12:13] offset0:16 offset1:24
	s_waitcnt vmcnt(7)
	v_cvt_pk_bf16_f32 v11, v36, v37
	v_cvt_pk_bf16_f32 v10, v34, v35
	s_waitcnt vmcnt(6)
	v_cvt_pk_bf16_f32 v13, v40, v41
	v_cvt_pk_bf16_f32 v12, v38, v39
	ds_write2st64_b64 v239, v[10:11], v[12:13] offset0:32 offset1:40
	s_waitcnt vmcnt(5)
	v_cvt_pk_bf16_f32 v11, v44, v45
	v_cvt_pk_bf16_f32 v10, v42, v43
	s_waitcnt vmcnt(4)
	v_cvt_pk_bf16_f32 v13, v48, v49
	v_cvt_pk_bf16_f32 v12, v46, v47
	ds_write2st64_b64 v239, v[10:11], v[12:13] offset0:48 offset1:56
	s_waitcnt lgkmcnt(0)
	s_add_i32 s21, s21, 2
	s_barrier
	s_waitcnt lgkmcnt(11)
	v_mfma_f32_16x16x32_bf16 v[174:177], v[178:181], v[206:209], v[174:177]
	s_lshl_b32 s22, s21, 1
	s_and_b32 s22, s22, 0x60
	s_add_i32 s22, s22, s12
	s_lshl_b32 s22, s22, 6
	v_mfma_f32_16x16x32_bf16 v[170:173], v[194:197], v[206:209], v[170:173]
	s_and_b32 s22, s22, 0x3f00
	s_or_b32 s22, s22, s13
	s_lshl_b32 s23, s21, 23
	s_lshl_b32 s22, s22, 9
	v_mfma_f32_16x16x32_bf16 v[158:161], v[198:201], v[206:209], v[158:161]
	s_and_b32 s23, s23, 0x7000000
	s_or_b32 s22, s22, s23
	s_lshl_b32 s23, s21, 8
	s_and_b32 s23, s23, 0x100
	s_or_b32 s22, s22, s23
	s_or_b32 s23, s22, 0x4000
	buffer_load_dwordx4 v[10:13], v1, s[4:7], s22 offen sc0 nt
	v_mfma_f32_16x16x32_bf16 v[142:145], v[202:205], v[206:209], v[142:145]
	s_waitcnt lgkmcnt(10)
	v_mfma_f32_16x16x32_bf16 v[166:169], v[178:181], v[210:213], v[166:169]
	v_mfma_f32_16x16x32_bf16 v[162:165], v[194:197], v[210:213], v[162:165]
	v_mfma_f32_16x16x32_bf16 v[146:149], v[198:201], v[210:213], v[146:149]
	buffer_load_dwordx4 v[18:21], v1, s[4:7], s23 offen sc0 nt
	s_or_b32 s23, s22, 0x8000
	v_mfma_f32_16x16x32_bf16 v[122:125], v[202:205], v[210:213], v[122:125]
	s_waitcnt lgkmcnt(9)
	v_mfma_f32_16x16x32_bf16 v[154:157], v[178:181], v[214:217], v[154:157]
	v_mfma_f32_16x16x32_bf16 v[150:153], v[194:197], v[214:217], v[150:153]
	v_mfma_f32_16x16x32_bf16 v[130:133], v[198:201], v[214:217], v[130:133]
	buffer_load_dwordx4 v[22:25], v1, s[4:7], s23 offen sc0 nt
	s_or_b32 s23, s22, 0xc000
	v_mfma_f32_16x16x32_bf16 v[106:109], v[202:205], v[214:217], v[106:109]
	s_waitcnt lgkmcnt(8)
	v_mfma_f32_16x16x32_bf16 v[138:141], v[178:181], v[218:221], v[138:141]
	v_mfma_f32_16x16x32_bf16 v[134:137], v[194:197], v[218:221], v[134:137]
	v_mfma_f32_16x16x32_bf16 v[114:117], v[198:201], v[218:221], v[114:117]
	buffer_load_dwordx4 v[30:33], v1, s[4:7], s23 offen sc0 nt
	s_or_b32 s23, s22, 0x10000
	v_mfma_f32_16x16x32_bf16 v[90:93], v[202:205], v[218:221], v[90:93]
	s_waitcnt lgkmcnt(7)
	v_mfma_f32_16x16x32_bf16 v[126:129], v[178:181], v[222:225], v[126:129]
	v_mfma_f32_16x16x32_bf16 v[118:121], v[194:197], v[222:225], v[118:121]
	v_mfma_f32_16x16x32_bf16 v[98:101], v[198:201], v[222:225], v[98:101]
	buffer_load_dwordx4 v[34:37], v1, s[4:7], s23 offen sc0 nt
	s_or_b32 s23, s22, 0x14000
	v_mfma_f32_16x16x32_bf16 v[74:77], v[202:205], v[222:225], v[74:77]
	s_waitcnt lgkmcnt(6)
	v_mfma_f32_16x16x32_bf16 v[110:113], v[178:181], v[226:229], v[110:113]
	v_mfma_f32_16x16x32_bf16 v[102:105], v[194:197], v[226:229], v[102:105]
	v_mfma_f32_16x16x32_bf16 v[82:85], v[198:201], v[226:229], v[82:85]
	buffer_load_dwordx4 v[38:41], v1, s[4:7], s23 offen sc0 nt
	s_or_b32 s23, s22, 0x18000
	s_or_b32 s22, s22, 0x1c000
	v_mfma_f32_16x16x32_bf16 v[62:65], v[202:205], v[226:229], v[62:65]
	s_waitcnt lgkmcnt(5)
	v_mfma_f32_16x16x32_bf16 v[94:97], v[178:181], v[230:233], v[94:97]
	v_mfma_f32_16x16x32_bf16 v[86:89], v[194:197], v[230:233], v[86:89]
	v_mfma_f32_16x16x32_bf16 v[70:73], v[198:201], v[230:233], v[70:73]
	buffer_load_dwordx4 v[42:45], v1, s[4:7], s23 offen sc0 nt
	v_mfma_f32_16x16x32_bf16 v[54:57], v[202:205], v[230:233], v[54:57]
	s_waitcnt lgkmcnt(4)
	v_mfma_f32_16x16x32_bf16 v[78:81], v[178:181], v[234:237], v[78:81]
	v_mfma_f32_16x16x32_bf16 v[66:69], v[194:197], v[234:237], v[66:69]
	v_mfma_f32_16x16x32_bf16 v[58:61], v[198:201], v[234:237], v[58:61]
	buffer_load_dwordx4 v[46:49], v1, s[4:7], s22 offen sc0 nt
	v_mfma_f32_16x16x32_bf16 v[50:53], v[202:205], v[234:237], v[50:53]
	s_waitcnt lgkmcnt(0)
	s_barrier
	ds_read_b128 v[178:181], v182 offset:33792
	ds_read_b128 v[194:197], v182 offset:35840
	ds_read_b128 v[198:201], v182 offset:37888
	ds_read_b128 v[202:205], v182 offset:39936
	ds_read_b128 v[206:209], v238 offset:1024
	ds_read_b128 v[210:213], v238 offset:3072
	ds_read_b128 v[214:217], v238 offset:5120
	ds_read_b128 v[218:221], v238 offset:7168
	ds_read_b128 v[222:225], v238 offset:9216
	ds_read_b128 v[226:229], v238 offset:11264
	ds_read_b128 v[230:233], v238 offset:13312
	ds_read_b128 v[234:237], v238 offset:15360
	v_add_u32_e32 v182, s19, v190
	s_waitcnt vmcnt(11)
	ds_write_b128 v182, v[2:5] offset:32768
	s_waitcnt vmcnt(10)
	ds_write_b128 v182, v[6:9] offset:40960
	s_waitcnt vmcnt(9)
	ds_write_b128 v182, v[14:17] offset:49152
	s_waitcnt vmcnt(8)
	ds_write_b128 v182, v[26:29] offset:57344
	s_waitcnt lgkmcnt(0)
	s_lshl_b32 s21, s21, 7
	s_and_b32 s21, s21, 0x780
	s_or_b32 s21, s21, s14
	s_or_b32 s22, s21, 0x20000
	buffer_load_dwordx4 v[2:5], v188, s[0:3], s21 offen sc1
	buffer_load_dwordx4 v[6:9], v188, s[0:3], s22 offen sc1
	s_or_b32 s22, s21, 0x40000
	s_or_b32 s21, s21, 0x60000
	buffer_load_dwordx4 v[14:17], v188, s[0:3], s22 offen sc1
	buffer_load_dwordx4 v[26:29], v188, s[0:3], s21 offen sc1
	s_barrier
	s_waitcnt lgkmcnt(11)
	v_mfma_f32_16x16x32_bf16 v[174:177], v[178:181], v[206:209], v[174:177]
	v_mfma_f32_16x16x32_bf16 v[170:173], v[194:197], v[206:209], v[170:173]
	v_mfma_f32_16x16x32_bf16 v[158:161], v[198:201], v[206:209], v[158:161]
	v_mfma_f32_16x16x32_bf16 v[142:145], v[202:205], v[206:209], v[142:145]
	s_waitcnt lgkmcnt(10)
	v_mfma_f32_16x16x32_bf16 v[166:169], v[178:181], v[210:213], v[166:169]
	v_mfma_f32_16x16x32_bf16 v[162:165], v[194:197], v[210:213], v[162:165]
	v_mfma_f32_16x16x32_bf16 v[146:149], v[198:201], v[210:213], v[146:149]
	v_mfma_f32_16x16x32_bf16 v[122:125], v[202:205], v[210:213], v[122:125]
	s_waitcnt lgkmcnt(9)
	v_mfma_f32_16x16x32_bf16 v[154:157], v[178:181], v[214:217], v[154:157]
	v_mfma_f32_16x16x32_bf16 v[150:153], v[194:197], v[214:217], v[150:153]
	v_mfma_f32_16x16x32_bf16 v[130:133], v[198:201], v[214:217], v[130:133]
	v_mfma_f32_16x16x32_bf16 v[106:109], v[202:205], v[214:217], v[106:109]
	s_waitcnt lgkmcnt(8)
	v_mfma_f32_16x16x32_bf16 v[138:141], v[178:181], v[218:221], v[138:141]
	v_mfma_f32_16x16x32_bf16 v[134:137], v[194:197], v[218:221], v[134:137]
	v_mfma_f32_16x16x32_bf16 v[114:117], v[198:201], v[218:221], v[114:117]
	v_mfma_f32_16x16x32_bf16 v[90:93], v[202:205], v[218:221], v[90:93]
	s_waitcnt lgkmcnt(7)
	v_mfma_f32_16x16x32_bf16 v[126:129], v[178:181], v[222:225], v[126:129]
	v_mfma_f32_16x16x32_bf16 v[118:121], v[194:197], v[222:225], v[118:121]
	v_mfma_f32_16x16x32_bf16 v[98:101], v[198:201], v[222:225], v[98:101]
	v_mfma_f32_16x16x32_bf16 v[74:77], v[202:205], v[222:225], v[74:77]
	s_waitcnt lgkmcnt(6)
	v_mfma_f32_16x16x32_bf16 v[110:113], v[178:181], v[226:229], v[110:113]
	v_mfma_f32_16x16x32_bf16 v[102:105], v[194:197], v[226:229], v[102:105]
	v_mfma_f32_16x16x32_bf16 v[82:85], v[198:201], v[226:229], v[82:85]
	v_mfma_f32_16x16x32_bf16 v[62:65], v[202:205], v[226:229], v[62:65]
	s_waitcnt lgkmcnt(5)
	v_mfma_f32_16x16x32_bf16 v[94:97], v[178:181], v[230:233], v[94:97]
	v_mfma_f32_16x16x32_bf16 v[86:89], v[194:197], v[230:233], v[86:89]
	v_mfma_f32_16x16x32_bf16 v[70:73], v[198:201], v[230:233], v[70:73]
	v_mfma_f32_16x16x32_bf16 v[54:57], v[202:205], v[230:233], v[54:57]
	s_waitcnt lgkmcnt(4)
	v_mfma_f32_16x16x32_bf16 v[78:81], v[178:181], v[234:237], v[78:81]
	v_mfma_f32_16x16x32_bf16 v[66:69], v[194:197], v[234:237], v[66:69]
	v_mfma_f32_16x16x32_bf16 v[58:61], v[198:201], v[234:237], v[58:61]
	v_mfma_f32_16x16x32_bf16 v[50:53], v[202:205], v[234:237], v[50:53]
	s_and_b32 s21, s20, 15
	s_cmp_lg_u32 s21, 15
	s_cbranch_scc1 .LBB1_3
	s_and_b32 s21, s18, 32
	s_add_i32 s21, s21, s12
	s_lshl_b32 s21, s21, 6
	s_and_b32 s21, s21, 0x3f00
	v_add_lshl_u32 v182, v193, s21, 9
	v_lshl_add_u64 v[206:207], v[184:185], 0, v[182:183]
	v_add_co_u32_e32 v208, vcc, s8, v206
	s_nop 1
	v_addc_co_u32_e32 v209, vcc, 0, v207, vcc
	v_add_co_u32_e32 v210, vcc, s15, v206
	s_nop 1
	v_addc_co_u32_e32 v211, vcc, 0, v207, vcc
	v_add_co_u32_e32 v212, vcc, s9, v206
	s_nop 1
	v_addc_co_u32_e32 v213, vcc, 0, v207, vcc
	v_add_co_u32_e32 v214, vcc, s16, v206
	s_nop 1
	v_addc_co_u32_e32 v215, vcc, 0, v207, vcc
	v_add_co_u32_e32 v216, vcc, s10, v206
	s_nop 1
	v_addc_co_u32_e32 v217, vcc, 0, v207, vcc
	v_add_co_u32_e32 v218, vcc, s17, v206
	s_nop 1
	v_addc_co_u32_e32 v219, vcc, 0, v207, vcc
	v_add_co_u32_e32 v220, vcc, s11, v206
	s_nop 1
	v_addc_co_u32_e32 v221, vcc, 0, v207, vcc
	global_store_dwordx4 v[206:207], v[174:177], off
	global_store_dwordx4 v[206:207], v[170:173], off offset:64
	global_store_dwordx4 v[206:207], v[158:161], off offset:128
	global_store_dwordx4 v[206:207], v[142:145], off offset:192
	global_store_dwordx4 v[208:209], v[166:169], off
	global_store_dwordx4 v[208:209], v[162:165], off offset:64
	global_store_dwordx4 v[208:209], v[146:149], off offset:128
	global_store_dwordx4 v[208:209], v[122:125], off offset:192
	global_store_dwordx4 v[210:211], v[154:157], off
	global_store_dwordx4 v[210:211], v[150:153], off offset:64
	global_store_dwordx4 v[210:211], v[130:133], off offset:128
	global_store_dwordx4 v[210:211], v[106:109], off offset:192
	global_store_dwordx4 v[212:213], v[138:141], off
	global_store_dwordx4 v[212:213], v[134:137], off offset:64
	global_store_dwordx4 v[212:213], v[114:117], off offset:128
	global_store_dwordx4 v[212:213], v[90:93], off offset:192
	global_store_dwordx4 v[214:215], v[126:129], off
	global_store_dwordx4 v[214:215], v[118:121], off offset:64
	global_store_dwordx4 v[214:215], v[98:101], off offset:128
	global_store_dwordx4 v[214:215], v[74:77], off offset:192
	global_store_dwordx4 v[216:217], v[110:113], off
	global_store_dwordx4 v[216:217], v[102:105], off offset:64
	global_store_dwordx4 v[216:217], v[82:85], off offset:128
	global_store_dwordx4 v[216:217], v[62:65], off offset:192
	global_store_dwordx4 v[218:219], v[94:97], off
	global_store_dwordx4 v[218:219], v[86:89], off offset:64
	global_store_dwordx4 v[218:219], v[70:73], off offset:128
	global_store_dwordx4 v[218:219], v[54:57], off offset:192
	global_store_dwordx4 v[220:221], v[78:81], off
	global_store_dwordx4 v[220:221], v[66:69], off offset:64
	global_store_dwordx4 v[220:221], v[58:61], off offset:128
	global_store_dwordx4 v[220:221], v[50:53], off offset:192
.Lpd_tail:
	s_waitcnt lgkmcnt(0)
	s_barrier
	s_add_i32 s20, s20, 1
	s_add_i32 s18, s18, 2
	v_add_u32_e32 v182, s19, v191
	v_add_u32_e32 v238, s19, v192
	ds_read_b128 v[178:181], v182 offset:32768
	ds_read_b128 v[194:197], v182 offset:34816
	ds_read_b128 v[198:201], v182 offset:36864
	ds_read_b128 v[202:205], v182 offset:38912
	ds_read_b128 v[206:209], v238
	ds_read_b128 v[210:213], v238 offset:2048
	ds_read_b128 v[214:217], v238 offset:4096
	ds_read_b128 v[218:221], v238 offset:6144
	ds_read_b128 v[222:225], v238 offset:8192
	ds_read_b128 v[226:229], v238 offset:10240
	ds_read_b128 v[230:233], v238 offset:12288
	ds_read_b128 v[234:237], v238 offset:14336
	s_min_u32 s21, s20, 29
	s_xor_b32 s19, s19, 0x10000
	v_add_u32_e32 v239, s19, v189
	s_waitcnt vmcnt(43)
	v_cvt_pk_bf16_f32 v13, v12, v13
	v_cvt_pk_bf16_f32 v12, v10, v11
	s_waitcnt vmcnt(42)
	v_cvt_pk_bf16_f32 v11, v20, v21
	v_cvt_pk_bf16_f32 v10, v18, v19
	ds_write2st64_b64 v239, v[12:13], v[10:11] offset1:8
	s_waitcnt vmcnt(41)
	v_cvt_pk_bf16_f32 v11, v24, v25
	v_cvt_pk_bf16_f32 v10, v22, v23
	s_waitcnt vmcnt(40)
	v_cvt_pk_bf16_f32 v13, v32, v33
	v_cvt_pk_bf16_f32 v12, v30, v31
	ds_write2st64_b64 v239, v[10:11], v[12:13] offset0:16 offset1:24
	s_waitcnt vmcnt(39)
	v_cvt_pk_bf16_f32 v11, v36, v37
	v_cvt_pk_bf16_f32 v10, v34, v35
	s_waitcnt vmcnt(38)
	v_cvt_pk_bf16_f32 v13, v40, v41
	v_cvt_pk_bf16_f32 v12, v38, v39
	ds_write2st64_b64 v239, v[10:11], v[12:13] offset0:32 offset1:40
	s_waitcnt vmcnt(37)
	v_cvt_pk_bf16_f32 v11, v44, v45
	v_cvt_pk_bf16_f32 v10, v42, v43
	s_waitcnt vmcnt(36)
	v_cvt_pk_bf16_f32 v13, v48, v49
	v_cvt_pk_bf16_f32 v12, v46, v47
	ds_write2st64_b64 v239, v[10:11], v[12:13] offset0:48 offset1:56
	s_waitcnt lgkmcnt(0)
	s_add_i32 s21, s21, 2
	s_barrier
	s_waitcnt lgkmcnt(11)
	v_mfma_f32_16x16x32_bf16 v[174:177], v[178:181], v[206:209], v[240:243]
	s_lshl_b32 s22, s21, 1
	s_and_b32 s22, s22, 0x60
	s_add_i32 s22, s22, s12
	s_lshl_b32 s22, s22, 6
	v_mfma_f32_16x16x32_bf16 v[170:173], v[194:197], v[206:209], v[244:247]
	s_and_b32 s22, s22, 0x3f00
	s_or_b32 s22, s22, s13
	s_lshl_b32 s23, s21, 23
	s_lshl_b32 s22, s22, 9
	v_mfma_f32_16x16x32_bf16 v[158:161], v[198:201], v[206:209], v[248:251]
	s_and_b32 s23, s23, 0x7000000
	s_or_b32 s22, s22, s23
	s_lshl_b32 s23, s21, 8
	s_and_b32 s23, s23, 0x100
	s_or_b32 s22, s22, s23
	s_or_b32 s23, s22, 0x4000
	buffer_load_dwordx4 v[10:13], v1, s[4:7], s22 offen sc0 nt
	v_mfma_f32_16x16x32_bf16 v[142:145], v[202:205], v[206:209], v[252:255]
	s_waitcnt lgkmcnt(10)
	v_mfma_f32_16x16x32_bf16 v[166:169], v[178:181], v[210:213], v[240:243]
	v_mfma_f32_16x16x32_bf16 v[162:165], v[194:197], v[210:213], v[244:247]
	v_mfma_f32_16x16x32_bf16 v[146:149], v[198:201], v[210:213], v[248:251]
	buffer_load_dwordx4 v[18:21], v1, s[4:7], s23 offen sc0 nt
	s_or_b32 s23, s22, 0x8000
	v_mfma_f32_16x16x32_bf16 v[122:125], v[202:205], v[210:213], v[252:255]
	s_waitcnt lgkmcnt(9)
	v_mfma_f32_16x16x32_bf16 v[154:157], v[178:181], v[214:217], v[240:243]
	v_mfma_f32_16x16x32_bf16 v[150:153], v[194:197], v[214:217], v[244:247]
	v_mfma_f32_16x16x32_bf16 v[130:133], v[198:201], v[214:217], v[248:251]
	buffer_load_dwordx4 v[22:25], v1, s[4:7], s23 offen sc0 nt
	s_or_b32 s23, s22, 0xc000
	v_mfma_f32_16x16x32_bf16 v[106:109], v[202:205], v[214:217], v[252:255]
	s_waitcnt lgkmcnt(8)
	v_mfma_f32_16x16x32_bf16 v[138:141], v[178:181], v[218:221], v[240:243]
	v_mfma_f32_16x16x32_bf16 v[134:137], v[194:197], v[218:221], v[244:247]
	v_mfma_f32_16x16x32_bf16 v[114:117], v[198:201], v[218:221], v[248:251]
	buffer_load_dwordx4 v[30:33], v1, s[4:7], s23 offen sc0 nt
	s_or_b32 s23, s22, 0x10000
	v_mfma_f32_16x16x32_bf16 v[90:93], v[202:205], v[218:221], v[252:255]
	s_waitcnt lgkmcnt(7)
	v_mfma_f32_16x16x32_bf16 v[126:129], v[178:181], v[222:225], v[240:243]
	v_mfma_f32_16x16x32_bf16 v[118:121], v[194:197], v[222:225], v[244:247]
	v_mfma_f32_16x16x32_bf16 v[98:101], v[198:201], v[222:225], v[248:251]
	buffer_load_dwordx4 v[34:37], v1, s[4:7], s23 offen sc0 nt
	s_or_b32 s23, s22, 0x14000
	v_mfma_f32_16x16x32_bf16 v[74:77], v[202:205], v[222:225], v[252:255]
	s_waitcnt lgkmcnt(6)
	v_mfma_f32_16x16x32_bf16 v[110:113], v[178:181], v[226:229], v[240:243]
	v_mfma_f32_16x16x32_bf16 v[102:105], v[194:197], v[226:229], v[244:247]
	v_mfma_f32_16x16x32_bf16 v[82:85], v[198:201], v[226:229], v[248:251]
	buffer_load_dwordx4 v[38:41], v1, s[4:7], s23 offen sc0 nt
	s_or_b32 s23, s22, 0x18000
	s_or_b32 s22, s22, 0x1c000
	v_mfma_f32_16x16x32_bf16 v[62:65], v[202:205], v[226:229], v[252:255]
	s_waitcnt lgkmcnt(5)
	v_mfma_f32_16x16x32_bf16 v[94:97], v[178:181], v[230:233], v[240:243]
	v_mfma_f32_16x16x32_bf16 v[86:89], v[194:197], v[230:233], v[244:247]
	v_mfma_f32_16x16x32_bf16 v[70:73], v[198:201], v[230:233], v[248:251]
	buffer_load_dwordx4 v[42:45], v1, s[4:7], s23 offen sc0 nt
	v_mfma_f32_16x16x32_bf16 v[54:57], v[202:205], v[230:233], v[252:255]
	s_waitcnt lgkmcnt(4)
	v_mfma_f32_16x16x32_bf16 v[78:81], v[178:181], v[234:237], v[240:243]
	v_mfma_f32_16x16x32_bf16 v[66:69], v[194:197], v[234:237], v[244:247]
	v_mfma_f32_16x16x32_bf16 v[58:61], v[198:201], v[234:237], v[248:251]
	buffer_load_dwordx4 v[46:49], v1, s[4:7], s22 offen sc0 nt
	v_mfma_f32_16x16x32_bf16 v[50:53], v[202:205], v[234:237], v[252:255]
	s_waitcnt lgkmcnt(0)
	s_barrier
	ds_read_b128 v[178:181], v182 offset:33792
	ds_read_b128 v[194:197], v182 offset:35840
	ds_read_b128 v[198:201], v182 offset:37888
	ds_read_b128 v[202:205], v182 offset:39936
	ds_read_b128 v[206:209], v238 offset:1024
	ds_read_b128 v[210:213], v238 offset:3072
	ds_read_b128 v[214:217], v238 offset:5120
	ds_read_b128 v[218:221], v238 offset:7168
	ds_read_b128 v[222:225], v238 offset:9216
	ds_read_b128 v[226:229], v238 offset:11264
	ds_read_b128 v[230:233], v238 offset:13312
	ds_read_b128 v[234:237], v238 offset:15360
	v_add_u32_e32 v182, s19, v190
	s_waitcnt vmcnt(43)
	ds_write_b128 v182, v[2:5] offset:32768
	s_waitcnt vmcnt(42)
	ds_write_b128 v182, v[6:9] offset:40960
	s_waitcnt vmcnt(41)
	ds_write_b128 v182, v[14:17] offset:49152
	s_waitcnt vmcnt(40)
	ds_write_b128 v182, v[26:29] offset:57344
	s_waitcnt lgkmcnt(0)
	s_lshl_b32 s21, s21, 7
	s_and_b32 s21, s21, 0x780
	s_or_b32 s21, s21, s14
	s_or_b32 s22, s21, 0x20000
	buffer_load_dwordx4 v[2:5], v188, s[0:3], s21 offen sc1
	buffer_load_dwordx4 v[6:9], v188, s[0:3], s22 offen sc1
	s_or_b32 s22, s21, 0x40000
	s_or_b32 s21, s21, 0x60000
	buffer_load_dwordx4 v[14:17], v188, s[0:3], s22 offen sc1
	buffer_load_dwordx4 v[26:29], v188, s[0:3], s21 offen sc1
	s_barrier
	s_waitcnt lgkmcnt(11)
	v_mfma_f32_16x16x32_bf16 v[174:177], v[178:181], v[206:209], v[174:177]
	v_mfma_f32_16x16x32_bf16 v[170:173], v[194:197], v[206:209], v[170:173]
	v_mfma_f32_16x16x32_bf16 v[158:161], v[198:201], v[206:209], v[158:161]
	v_mfma_f32_16x16x32_bf16 v[142:145], v[202:205], v[206:209], v[142:145]
	s_waitcnt lgkmcnt(10)
	v_mfma_f32_16x16x32_bf16 v[166:169], v[178:181], v[210:213], v[166:169]
	v_mfma_f32_16x16x32_bf16 v[162:165], v[194:197], v[210:213], v[162:165]
	v_mfma_f32_16x16x32_bf16 v[146:149], v[198:201], v[210:213], v[146:149]
	v_mfma_f32_16x16x32_bf16 v[122:125], v[202:205], v[210:213], v[122:125]
	s_waitcnt lgkmcnt(9)
	v_mfma_f32_16x16x32_bf16 v[154:157], v[178:181], v[214:217], v[154:157]
	v_mfma_f32_16x16x32_bf16 v[150:153], v[194:197], v[214:217], v[150:153]
	v_mfma_f32_16x16x32_bf16 v[130:133], v[198:201], v[214:217], v[130:133]
	v_mfma_f32_16x16x32_bf16 v[106:109], v[202:205], v[214:217], v[106:109]
	s_waitcnt lgkmcnt(8)
	v_mfma_f32_16x16x32_bf16 v[138:141], v[178:181], v[218:221], v[138:141]
	v_mfma_f32_16x16x32_bf16 v[134:137], v[194:197], v[218:221], v[134:137]
	v_mfma_f32_16x16x32_bf16 v[114:117], v[198:201], v[218:221], v[114:117]
	v_mfma_f32_16x16x32_bf16 v[90:93], v[202:205], v[218:221], v[90:93]
	s_waitcnt lgkmcnt(7)
	v_mfma_f32_16x16x32_bf16 v[126:129], v[178:181], v[222:225], v[126:129]
	v_mfma_f32_16x16x32_bf16 v[118:121], v[194:197], v[222:225], v[118:121]
	v_mfma_f32_16x16x32_bf16 v[98:101], v[198:201], v[222:225], v[98:101]
	v_mfma_f32_16x16x32_bf16 v[74:77], v[202:205], v[222:225], v[74:77]
	s_waitcnt lgkmcnt(6)
	v_mfma_f32_16x16x32_bf16 v[110:113], v[178:181], v[226:229], v[110:113]
	v_mfma_f32_16x16x32_bf16 v[102:105], v[194:197], v[226:229], v[102:105]
	v_mfma_f32_16x16x32_bf16 v[82:85], v[198:201], v[226:229], v[82:85]
	v_mfma_f32_16x16x32_bf16 v[62:65], v[202:205], v[226:229], v[62:65]
	s_waitcnt lgkmcnt(5)
	v_mfma_f32_16x16x32_bf16 v[94:97], v[178:181], v[230:233], v[94:97]
	v_mfma_f32_16x16x32_bf16 v[86:89], v[194:197], v[230:233], v[86:89]
	v_mfma_f32_16x16x32_bf16 v[70:73], v[198:201], v[230:233], v[70:73]
	v_mfma_f32_16x16x32_bf16 v[54:57], v[202:205], v[230:233], v[54:57]
	s_waitcnt lgkmcnt(4)
	v_mfma_f32_16x16x32_bf16 v[78:81], v[178:181], v[234:237], v[78:81]
	v_mfma_f32_16x16x32_bf16 v[66:69], v[194:197], v[234:237], v[66:69]
	v_mfma_f32_16x16x32_bf16 v[58:61], v[198:201], v[234:237], v[58:61]
	v_mfma_f32_16x16x32_bf16 v[50:53], v[202:205], v[234:237], v[50:53]
	s_branch .LBB1_3
.Lt30:
	v_add_u32_e32 v182, s19, v191
	v_add_u32_e32 v238, s19, v192
	ds_read_b128 v[178:181], v182 offset:32768
	ds_read_b128 v[194:197], v182 offset:34816
	ds_read_b128 v[198:201], v182 offset:36864
	ds_read_b128 v[202:205], v182 offset:38912
	ds_read_b128 v[206:209], v238
	ds_read_b128 v[210:213], v238 offset:2048
	ds_read_b128 v[214:217], v238 offset:4096
	ds_read_b128 v[218:221], v238 offset:6144
	ds_read_b128 v[222:225], v238 offset:8192
	ds_read_b128 v[226:229], v238 offset:10240
	ds_read_b128 v[230:233], v238 offset:12288
	ds_read_b128 v[234:237], v238 offset:14336
	s_min_u32 s21, s20, 29
	s_xor_b32 s19, s19, 0x10000
	v_add_u32_e32 v239, s19, v189
	s_waitcnt vmcnt(11)
	v_cvt_pk_bf16_f32 v13, v12, v13
	v_cvt_pk_bf16_f32 v12, v10, v11
	s_waitcnt vmcnt(10)
	v_cvt_pk_bf16_f32 v11, v20, v21
	v_cvt_pk_bf16_f32 v10, v18, v19
	ds_write2st64_b64 v239, v[12:13], v[10:11] offset1:8
	s_waitcnt vmcnt(9)
	v_cvt_pk_bf16_f32 v11, v24, v25
	v_cvt_pk_bf16_f32 v10, v22, v23
	s_waitcnt vmcnt(8)
	v_cvt_pk_bf16_f32 v13, v32, v33
	v_cvt_pk_bf16_f32 v12, v30, v31
	ds_write2st64_b64 v239, v[10:11], v[12:13] offset0:16 offset1:24
	s_waitcnt vmcnt(7)
	v_cvt_pk_bf16_f32 v11, v36, v37
	v_cvt_pk_bf16_f32 v10, v34, v35
	s_waitcnt vmcnt(6)
	v_cvt_pk_bf16_f32 v13, v40, v41
	v_cvt_pk_bf16_f32 v12, v38, v39
	ds_write2st64_b64 v239, v[10:11], v[12:13] offset0:32 offset1:40
	s_waitcnt vmcnt(5)
	v_cvt_pk_bf16_f32 v11, v44, v45
	v_cvt_pk_bf16_f32 v10, v42, v43
	s_waitcnt vmcnt(4)
	v_cvt_pk_bf16_f32 v13, v48, v49
	v_cvt_pk_bf16_f32 v12, v46, v47
	ds_write2st64_b64 v239, v[10:11], v[12:13] offset0:48 offset1:56
	s_waitcnt lgkmcnt(0)
	s_add_i32 s21, s21, 2
	s_barrier
	s_waitcnt lgkmcnt(11)
	v_mfma_f32_16x16x32_bf16 v[174:177], v[178:181], v[206:209], v[174:177]
	s_lshl_b32 s22, s21, 1
	s_and_b32 s22, s22, 0x60
	s_add_i32 s22, s22, s12
	s_lshl_b32 s22, s22, 6
	v_mfma_f32_16x16x32_bf16 v[170:173], v[194:197], v[206:209], v[170:173]
	s_and_b32 s22, s22, 0x3f00
	s_or_b32 s22, s22, s13
	s_lshl_b32 s23, s21, 23
	s_lshl_b32 s22, s22, 9
	v_mfma_f32_16x16x32_bf16 v[158:161], v[198:201], v[206:209], v[158:161]
	s_and_b32 s23, s23, 0x7000000
	s_or_b32 s22, s22, s23
	s_lshl_b32 s23, s21, 8
	s_and_b32 s23, s23, 0x100
	s_or_b32 s22, s22, s23
	s_or_b32 s23, s22, 0x4000
	v_mfma_f32_16x16x32_bf16 v[142:145], v[202:205], v[206:209], v[142:145]
	s_waitcnt lgkmcnt(10)
	v_mfma_f32_16x16x32_bf16 v[166:169], v[178:181], v[210:213], v[166:169]
	v_mfma_f32_16x16x32_bf16 v[162:165], v[194:197], v[210:213], v[162:165]
	v_mfma_f32_16x16x32_bf16 v[146:149], v[198:201], v[210:213], v[146:149]
	s_or_b32 s23, s22, 0x8000
	v_mfma_f32_16x16x32_bf16 v[122:125], v[202:205], v[210:213], v[122:125]
	s_waitcnt lgkmcnt(9)
	v_mfma_f32_16x16x32_bf16 v[154:157], v[178:181], v[214:217], v[154:157]
	v_mfma_f32_16x16x32_bf16 v[150:153], v[194:197], v[214:217], v[150:153]
	v_mfma_f32_16x16x32_bf16 v[130:133], v[198:201], v[214:217], v[130:133]
	s_or_b32 s23, s22, 0xc000
	v_mfma_f32_16x16x32_bf16 v[106:109], v[202:205], v[214:217], v[106:109]
	s_waitcnt lgkmcnt(8)
	v_mfma_f32_16x16x32_bf16 v[138:141], v[178:181], v[218:221], v[138:141]
	v_mfma_f32_16x16x32_bf16 v[134:137], v[194:197], v[218:221], v[134:137]
	v_mfma_f32_16x16x32_bf16 v[114:117], v[198:201], v[218:221], v[114:117]
	s_or_b32 s23, s22, 0x10000
	v_mfma_f32_16x16x32_bf16 v[90:93], v[202:205], v[218:221], v[90:93]
	s_waitcnt lgkmcnt(7)
	v_mfma_f32_16x16x32_bf16 v[126:129], v[178:181], v[222:225], v[126:129]
	v_mfma_f32_16x16x32_bf16 v[118:121], v[194:197], v[222:225], v[118:121]
	v_mfma_f32_16x16x32_bf16 v[98:101], v[198:201], v[222:225], v[98:101]
	s_or_b32 s23, s22, 0x14000
	v_mfma_f32_16x16x32_bf16 v[74:77], v[202:205], v[222:225], v[74:77]
	s_waitcnt lgkmcnt(6)
	v_mfma_f32_16x16x32_bf16 v[110:113], v[178:181], v[226:229], v[110:113]
	v_mfma_f32_16x16x32_bf16 v[102:105], v[194:197], v[226:229], v[102:105]
	v_mfma_f32_16x16x32_bf16 v[82:85], v[198:201], v[226:229], v[82:85]
	s_or_b32 s23, s22, 0x18000
	s_or_b32 s22, s22, 0x1c000
	v_mfma_f32_16x16x32_bf16 v[62:65], v[202:205], v[226:229], v[62:65]
	s_waitcnt lgkmcnt(5)
	v_mfma_f32_16x16x32_bf16 v[94:97], v[178:181], v[230:233], v[94:97]
	v_mfma_f32_16x16x32_bf16 v[86:89], v[194:197], v[230:233], v[86:89]
	v_mfma_f32_16x16x32_bf16 v[70:73], v[198:201], v[230:233], v[70:73]
	v_mfma_f32_16x16x32_bf16 v[54:57], v[202:205], v[230:233], v[54:57]
	s_waitcnt lgkmcnt(4)
	v_mfma_f32_16x16x32_bf16 v[78:81], v[178:181], v[234:237], v[78:81]
	v_mfma_f32_16x16x32_bf16 v[66:69], v[194:197], v[234:237], v[66:69]
	v_mfma_f32_16x16x32_bf16 v[58:61], v[198:201], v[234:237], v[58:61]
	v_mfma_f32_16x16x32_bf16 v[50:53], v[202:205], v[234:237], v[50:53]
	s_waitcnt lgkmcnt(0)
	s_barrier
	ds_read_b128 v[178:181], v182 offset:33792
	ds_read_b128 v[194:197], v182 offset:35840
	ds_read_b128 v[198:201], v182 offset:37888
	ds_read_b128 v[202:205], v182 offset:39936
	ds_read_b128 v[206:209], v238 offset:1024
	ds_read_b128 v[210:213], v238 offset:3072
	ds_read_b128 v[214:217], v238 offset:5120
	ds_read_b128 v[218:221], v238 offset:7168
	ds_read_b128 v[222:225], v238 offset:9216
	ds_read_b128 v[226:229], v238 offset:11264
	ds_read_b128 v[230:233], v238 offset:13312
	ds_read_b128 v[234:237], v238 offset:15360
	v_add_u32_e32 v182, s19, v190
	s_waitcnt vmcnt(3)
	ds_write_b128 v182, v[2:5] offset:32768
	s_waitcnt vmcnt(2)
	ds_write_b128 v182, v[6:9] offset:40960
	s_waitcnt vmcnt(1)
	ds_write_b128 v182, v[14:17] offset:49152
	s_waitcnt vmcnt(0)
	ds_write_b128 v182, v[26:29] offset:57344
	s_waitcnt lgkmcnt(0)
	s_lshl_b32 s21, s21, 7
	s_and_b32 s21, s21, 0x780
	s_or_b32 s21, s21, s14
	s_or_b32 s22, s21, 0x20000
	s_or_b32 s22, s21, 0x40000
	s_or_b32 s21, s21, 0x60000
	s_barrier
	s_waitcnt lgkmcnt(11)
	v_mfma_f32_16x16x32_bf16 v[174:177], v[178:181], v[206:209], v[174:177]
	v_mfma_f32_16x16x32_bf16 v[170:173], v[194:197], v[206:209], v[170:173]
	v_mfma_f32_16x16x32_bf16 v[158:161], v[198:201], v[206:209], v[158:161]
	v_mfma_f32_16x16x32_bf16 v[142:145], v[202:205], v[206:209], v[142:145]
	s_waitcnt lgkmcnt(10)
	v_mfma_f32_16x16x32_bf16 v[166:169], v[178:181], v[210:213], v[166:169]
	v_mfma_f32_16x16x32_bf16 v[162:165], v[194:197], v[210:213], v[162:165]
	v_mfma_f32_16x16x32_bf16 v[146:149], v[198:201], v[210:213], v[146:149]
	v_mfma_f32_16x16x32_bf16 v[122:125], v[202:205], v[210:213], v[122:125]
	s_waitcnt lgkmcnt(9)
	v_mfma_f32_16x16x32_bf16 v[154:157], v[178:181], v[214:217], v[154:157]
	v_mfma_f32_16x16x32_bf16 v[150:153], v[194:197], v[214:217], v[150:153]
	v_mfma_f32_16x16x32_bf16 v[130:133], v[198:201], v[214:217], v[130:133]
	v_mfma_f32_16x16x32_bf16 v[106:109], v[202:205], v[214:217], v[106:109]
	s_waitcnt lgkmcnt(8)
	v_mfma_f32_16x16x32_bf16 v[138:141], v[178:181], v[218:221], v[138:141]
	v_mfma_f32_16x16x32_bf16 v[134:137], v[194:197], v[218:221], v[134:137]
	v_mfma_f32_16x16x32_bf16 v[114:117], v[198:201], v[218:221], v[114:117]
	v_mfma_f32_16x16x32_bf16 v[90:93], v[202:205], v[218:221], v[90:93]
	s_waitcnt lgkmcnt(7)
	v_mfma_f32_16x16x32_bf16 v[126:129], v[178:181], v[222:225], v[126:129]
	v_mfma_f32_16x16x32_bf16 v[118:121], v[194:197], v[222:225], v[118:121]
	v_mfma_f32_16x16x32_bf16 v[98:101], v[198:201], v[222:225], v[98:101]
	v_mfma_f32_16x16x32_bf16 v[74:77], v[202:205], v[222:225], v[74:77]
	s_waitcnt lgkmcnt(6)
	v_mfma_f32_16x16x32_bf16 v[110:113], v[178:181], v[226:229], v[110:113]
	v_mfma_f32_16x16x32_bf16 v[102:105], v[194:197], v[226:229], v[102:105]
	v_mfma_f32_16x16x32_bf16 v[82:85], v[198:201], v[226:229], v[82:85]
	v_mfma_f32_16x16x32_bf16 v[62:65], v[202:205], v[226:229], v[62:65]
	s_waitcnt lgkmcnt(5)
	v_mfma_f32_16x16x32_bf16 v[94:97], v[178:181], v[230:233], v[94:97]
	v_mfma_f32_16x16x32_bf16 v[86:89], v[194:197], v[230:233], v[86:89]
	v_mfma_f32_16x16x32_bf16 v[70:73], v[198:201], v[230:233], v[70:73]
	v_mfma_f32_16x16x32_bf16 v[54:57], v[202:205], v[230:233], v[54:57]
	s_waitcnt lgkmcnt(4)
	v_mfma_f32_16x16x32_bf16 v[78:81], v[178:181], v[234:237], v[78:81]
	v_mfma_f32_16x16x32_bf16 v[66:69], v[194:197], v[234:237], v[66:69]
	v_mfma_f32_16x16x32_bf16 v[58:61], v[198:201], v[234:237], v[58:61]
	v_mfma_f32_16x16x32_bf16 v[50:53], v[202:205], v[234:237], v[50:53]
	s_waitcnt lgkmcnt(0)
	s_barrier
	s_add_i32 s20, s20, 1
	s_add_i32 s18, s18, 2
	v_add_u32_e32 v182, s19, v191
	v_add_u32_e32 v238, s19, v192
	ds_read_b128 v[178:181], v182 offset:32768
	ds_read_b128 v[194:197], v182 offset:34816
	ds_read_b128 v[198:201], v182 offset:36864
	ds_read_b128 v[202:205], v182 offset:38912
	ds_read_b128 v[206:209], v238
	ds_read_b128 v[210:213], v238 offset:2048
	ds_read_b128 v[214:217], v238 offset:4096
	ds_read_b128 v[218:221], v238 offset:6144
	ds_read_b128 v[222:225], v238 offset:8192
	ds_read_b128 v[226:229], v238 offset:10240
	ds_read_b128 v[230:233], v238 offset:12288
	ds_read_b128 v[234:237], v238 offset:14336
	s_min_u32 s21, s20, 29
	s_xor_b32 s19, s19, 0x10000
	v_add_u32_e32 v239, s19, v189
	s_waitcnt lgkmcnt(0)
	s_add_i32 s21, s21, 2
	s_barrier
	s_waitcnt lgkmcnt(11)
	v_mfma_f32_16x16x32_bf16 v[174:177], v[178:181], v[206:209], v[174:177]
	s_lshl_b32 s22, s21, 1
	s_and_b32 s22, s22, 0x60
	s_add_i32 s22, s22, s12
	s_lshl_b32 s22, s22, 6
	v_mfma_f32_16x16x32_bf16 v[170:173], v[194:197], v[206:209], v[170:173]
	s_and_b32 s22, s22, 0x3f00
	s_or_b32 s22, s22, s13
	s_lshl_b32 s23, s21, 23
	s_lshl_b32 s22, s22, 9
	v_mfma_f32_16x16x32_bf16 v[158:161], v[198:201], v[206:209], v[158:161]
	s_and_b32 s23, s23, 0x7000000
	s_or_b32 s22, s22, s23
	s_lshl_b32 s23, s21, 8
	s_and_b32 s23, s23, 0x100
	s_or_b32 s22, s22, s23
	s_or_b32 s23, s22, 0x4000
	v_mfma_f32_16x16x32_bf16 v[142:145], v[202:205], v[206:209], v[142:145]
	s_waitcnt lgkmcnt(10)
	v_mfma_f32_16x16x32_bf16 v[166:169], v[178:181], v[210:213], v[166:169]
	v_mfma_f32_16x16x32_bf16 v[162:165], v[194:197], v[210:213], v[162:165]
	v_mfma_f32_16x16x32_bf16 v[146:149], v[198:201], v[210:213], v[146:149]
	s_or_b32 s23, s22, 0x8000
	v_mfma_f32_16x16x32_bf16 v[122:125], v[202:205], v[210:213], v[122:125]
	s_waitcnt lgkmcnt(9)
	v_mfma_f32_16x16x32_bf16 v[154:157], v[178:181], v[214:217], v[154:157]
	v_mfma_f32_16x16x32_bf16 v[150:153], v[194:197], v[214:217], v[150:153]
	v_mfma_f32_16x16x32_bf16 v[130:133], v[198:201], v[214:217], v[130:133]
	s_or_b32 s23, s22, 0xc000
	v_mfma_f32_16x16x32_bf16 v[106:109], v[202:205], v[214:217], v[106:109]
	s_waitcnt lgkmcnt(8)
	v_mfma_f32_16x16x32_bf16 v[138:141], v[178:181], v[218:221], v[138:141]
	v_mfma_f32_16x16x32_bf16 v[134:137], v[194:197], v[218:221], v[134:137]
	v_mfma_f32_16x16x32_bf16 v[114:117], v[198:201], v[218:221], v[114:117]
	s_or_b32 s23, s22, 0x10000
	v_mfma_f32_16x16x32_bf16 v[90:93], v[202:205], v[218:221], v[90:93]
	s_waitcnt lgkmcnt(7)
	v_mfma_f32_16x16x32_bf16 v[126:129], v[178:181], v[222:225], v[126:129]
	v_mfma_f32_16x16x32_bf16 v[118:121], v[194:197], v[222:225], v[118:121]
	v_mfma_f32_16x16x32_bf16 v[98:101], v[198:201], v[222:225], v[98:101]
	s_or_b32 s23, s22, 0x14000
	v_mfma_f32_16x16x32_bf16 v[74:77], v[202:205], v[222:225], v[74:77]
	s_waitcnt lgkmcnt(6)
	v_mfma_f32_16x16x32_bf16 v[110:113], v[178:181], v[226:229], v[110:113]
	v_mfma_f32_16x16x32_bf16 v[102:105], v[194:197], v[226:229], v[102:105]
	v_mfma_f32_16x16x32_bf16 v[82:85], v[198:201], v[226:229], v[82:85]
	s_or_b32 s23, s22, 0x18000
	s_or_b32 s22, s22, 0x1c000
	v_mfma_f32_16x16x32_bf16 v[62:65], v[202:205], v[226:229], v[62:65]
	s_waitcnt lgkmcnt(5)
	v_mfma_f32_16x16x32_bf16 v[94:97], v[178:181], v[230:233], v[94:97]
	v_mfma_f32_16x16x32_bf16 v[86:89], v[194:197], v[230:233], v[86:89]
	v_mfma_f32_16x16x32_bf16 v[70:73], v[198:201], v[230:233], v[70:73]
	v_mfma_f32_16x16x32_bf16 v[54:57], v[202:205], v[230:233], v[54:57]
	s_waitcnt lgkmcnt(4)
	v_mfma_f32_16x16x32_bf16 v[78:81], v[178:181], v[234:237], v[78:81]
	v_mfma_f32_16x16x32_bf16 v[66:69], v[194:197], v[234:237], v[66:69]
	v_mfma_f32_16x16x32_bf16 v[58:61], v[198:201], v[234:237], v[58:61]
	v_mfma_f32_16x16x32_bf16 v[50:53], v[202:205], v[234:237], v[50:53]
	s_waitcnt lgkmcnt(0)
	s_barrier
	ds_read_b128 v[178:181], v182 offset:33792
	ds_read_b128 v[194:197], v182 offset:35840
	ds_read_b128 v[198:201], v182 offset:37888
	ds_read_b128 v[202:205], v182 offset:39936
	ds_read_b128 v[206:209], v238 offset:1024
	ds_read_b128 v[210:213], v238 offset:3072
	ds_read_b128 v[214:217], v238 offset:5120
	ds_read_b128 v[218:221], v238 offset:7168
	ds_read_b128 v[222:225], v238 offset:9216
	ds_read_b128 v[226:229], v238 offset:11264
	ds_read_b128 v[230:233], v238 offset:13312
	ds_read_b128 v[234:237], v238 offset:15360
	s_waitcnt lgkmcnt(0)
	s_lshl_b32 s21, s21, 7
	s_and_b32 s21, s21, 0x780
	s_or_b32 s21, s21, s14
	s_or_b32 s22, s21, 0x20000
	s_or_b32 s22, s21, 0x40000
	s_or_b32 s21, s21, 0x60000
	s_barrier
	s_waitcnt lgkmcnt(11)
	v_mfma_f32_16x16x32_bf16 v[174:177], v[178:181], v[206:209], v[174:177]
	v_mfma_f32_16x16x32_bf16 v[170:173], v[194:197], v[206:209], v[170:173]
	v_mfma_f32_16x16x32_bf16 v[158:161], v[198:201], v[206:209], v[158:161]
	v_mfma_f32_16x16x32_bf16 v[142:145], v[202:205], v[206:209], v[142:145]
	s_waitcnt lgkmcnt(10)
	v_mfma_f32_16x16x32_bf16 v[166:169], v[178:181], v[210:213], v[166:169]
	v_mfma_f32_16x16x32_bf16 v[162:165], v[194:197], v[210:213], v[162:165]
	v_mfma_f32_16x16x32_bf16 v[146:149], v[198:201], v[210:213], v[146:149]
	v_mfma_f32_16x16x32_bf16 v[122:125], v[202:205], v[210:213], v[122:125]
	s_waitcnt lgkmcnt(9)
	v_mfma_f32_16x16x32_bf16 v[154:157], v[178:181], v[214:217], v[154:157]
	v_mfma_f32_16x16x32_bf16 v[150:153], v[194:197], v[214:217], v[150:153]
	v_mfma_f32_16x16x32_bf16 v[130:133], v[198:201], v[214:217], v[130:133]
	v_mfma_f32_16x16x32_bf16 v[106:109], v[202:205], v[214:217], v[106:109]
	s_waitcnt lgkmcnt(8)
	v_mfma_f32_16x16x32_bf16 v[138:141], v[178:181], v[218:221], v[138:141]
	v_mfma_f32_16x16x32_bf16 v[134:137], v[194:197], v[218:221], v[134:137]
	v_mfma_f32_16x16x32_bf16 v[114:117], v[198:201], v[218:221], v[114:117]
	v_mfma_f32_16x16x32_bf16 v[90:93], v[202:205], v[218:221], v[90:93]
	s_waitcnt lgkmcnt(7)
	v_mfma_f32_16x16x32_bf16 v[126:129], v[178:181], v[222:225], v[126:129]
	v_mfma_f32_16x16x32_bf16 v[118:121], v[194:197], v[222:225], v[118:121]
	v_mfma_f32_16x16x32_bf16 v[98:101], v[198:201], v[222:225], v[98:101]
	v_mfma_f32_16x16x32_bf16 v[74:77], v[202:205], v[222:225], v[74:77]
	s_waitcnt lgkmcnt(6)
	v_mfma_f32_16x16x32_bf16 v[110:113], v[178:181], v[226:229], v[110:113]
	v_mfma_f32_16x16x32_bf16 v[102:105], v[194:197], v[226:229], v[102:105]
	v_mfma_f32_16x16x32_bf16 v[82:85], v[198:201], v[226:229], v[82:85]
	v_mfma_f32_16x16x32_bf16 v[62:65], v[202:205], v[226:229], v[62:65]
	s_waitcnt lgkmcnt(5)
	v_mfma_f32_16x16x32_bf16 v[94:97], v[178:181], v[230:233], v[94:97]
	v_mfma_f32_16x16x32_bf16 v[86:89], v[194:197], v[230:233], v[86:89]
	v_mfma_f32_16x16x32_bf16 v[70:73], v[198:201], v[230:233], v[70:73]
	v_mfma_f32_16x16x32_bf16 v[54:57], v[202:205], v[230:233], v[54:57]
	s_waitcnt lgkmcnt(4)
	v_mfma_f32_16x16x32_bf16 v[78:81], v[178:181], v[234:237], v[78:81]
	v_mfma_f32_16x16x32_bf16 v[66:69], v[194:197], v[234:237], v[66:69]
	v_mfma_f32_16x16x32_bf16 v[58:61], v[198:201], v[234:237], v[58:61]
	v_mfma_f32_16x16x32_bf16 v[50:53], v[202:205], v[234:237], v[50:53]
	s_and_b32 s21, s18, 32
	s_add_i32 s21, s21, s12
	s_lshl_b32 s21, s21, 6
	s_and_b32 s21, s21, 0x3f00
	v_add_lshl_u32 v182, v193, s21, 9
	v_lshl_add_u64 v[206:207], v[184:185], 0, v[182:183]
	v_add_co_u32_e32 v208, vcc, s8, v206
	s_nop 1
	v_addc_co_u32_e32 v209, vcc, 0, v207, vcc
	v_add_co_u32_e32 v210, vcc, s15, v206
	s_nop 1
	v_addc_co_u32_e32 v211, vcc, 0, v207, vcc
	v_add_co_u32_e32 v212, vcc, s9, v206
	s_nop 1
	v_addc_co_u32_e32 v213, vcc, 0, v207, vcc
	v_add_co_u32_e32 v214, vcc, s16, v206
	s_nop 1
	v_addc_co_u32_e32 v215, vcc, 0, v207, vcc
	v_add_co_u32_e32 v216, vcc, s10, v206
	s_nop 1
	v_addc_co_u32_e32 v217, vcc, 0, v207, vcc
	v_add_co_u32_e32 v218, vcc, s17, v206
	s_nop 1
	v_addc_co_u32_e32 v219, vcc, 0, v207, vcc
	v_add_co_u32_e32 v220, vcc, s11, v206
	s_nop 1
	v_addc_co_u32_e32 v221, vcc, 0, v207, vcc
	global_store_dwordx4 v[206:207], v[174:177], off
	global_store_dwordx4 v[206:207], v[170:173], off offset:64
	global_store_dwordx4 v[206:207], v[158:161], off offset:128
	global_store_dwordx4 v[206:207], v[142:145], off offset:192
	global_store_dwordx4 v[208:209], v[166:169], off
	global_store_dwordx4 v[208:209], v[162:165], off offset:64
	global_store_dwordx4 v[208:209], v[146:149], off offset:128
	global_store_dwordx4 v[208:209], v[122:125], off offset:192
	global_store_dwordx4 v[210:211], v[154:157], off
	global_store_dwordx4 v[210:211], v[150:153], off offset:64
	global_store_dwordx4 v[210:211], v[130:133], off offset:128
	global_store_dwordx4 v[210:211], v[106:109], off offset:192
	global_store_dwordx4 v[212:213], v[138:141], off
	global_store_dwordx4 v[212:213], v[134:137], off offset:64
	global_store_dwordx4 v[212:213], v[114:117], off offset:128
	global_store_dwordx4 v[212:213], v[90:93], off offset:192
	global_store_dwordx4 v[214:215], v[126:129], off
	global_store_dwordx4 v[214:215], v[118:121], off offset:64
	global_store_dwordx4 v[214:215], v[98:101], off offset:128
	global_store_dwordx4 v[214:215], v[74:77], off offset:192
	global_store_dwordx4 v[216:217], v[110:113], off
	global_store_dwordx4 v[216:217], v[102:105], off offset:64
	global_store_dwordx4 v[216:217], v[82:85], off offset:128
	global_store_dwordx4 v[216:217], v[62:65], off offset:192
	global_store_dwordx4 v[218:219], v[94:97], off
	global_store_dwordx4 v[218:219], v[86:89], off offset:64
	global_store_dwordx4 v[218:219], v[70:73], off offset:128
	global_store_dwordx4 v[218:219], v[54:57], off offset:192
	global_store_dwordx4 v[220:221], v[78:81], off
	global_store_dwordx4 v[220:221], v[66:69], off offset:64
	global_store_dwordx4 v[220:221], v[58:61], off offset:128
	global_store_dwordx4 v[220:221], v[50:53], off offset:192
	s_waitcnt lgkmcnt(0)
	s_barrier
	s_branch .LBB1_6
.Lfirst:
	v_add_u32_e32 v182, s19, v191
	v_add_u32_e32 v238, s19, v192
	ds_read_b128 v[178:181], v182 offset:32768
	ds_read_b128 v[194:197], v182 offset:34816
	ds_read_b128 v[198:201], v182 offset:36864
	ds_read_b128 v[202:205], v182 offset:38912
	ds_read_b128 v[206:209], v238
	ds_read_b128 v[210:213], v238 offset:2048
	ds_read_b128 v[214:217], v238 offset:4096
	ds_read_b128 v[218:221], v238 offset:6144
	ds_read_b128 v[222:225], v238 offset:8192
	ds_read_b128 v[226:229], v238 offset:10240
	ds_read_b128 v[230:233], v238 offset:12288
	ds_read_b128 v[234:237], v238 offset:14336
	s_min_u32 s21, s20, 29
	s_xor_b32 s19, s19, 0x10000
	v_add_u32_e32 v239, s19, v189
	s_waitcnt vmcnt(11)
	v_cvt_pk_bf16_f32 v13, v12, v13
	v_cvt_pk_bf16_f32 v12, v10, v11
	s_waitcnt vmcnt(10)
	v_cvt_pk_bf16_f32 v11, v20, v21
	v_cvt_pk_bf16_f32 v10, v18, v19
	ds_write2st64_b64 v239, v[12:13], v[10:11] offset1:8
	s_waitcnt vmcnt(9)
	v_cvt_pk_bf16_f32 v11, v24, v25
	v_cvt_pk_bf16_f32 v10, v22, v23
	s_waitcnt vmcnt(8)
	v_cvt_pk_bf16_f32 v13, v32, v33
	v_cvt_pk_bf16_f32 v12, v30, v31
	ds_write2st64_b64 v239, v[10:11], v[12:13] offset0:16 offset1:24
	s_waitcnt vmcnt(7)
	v_cvt_pk_bf16_f32 v11, v36, v37
	v_cvt_pk_bf16_f32 v10, v34, v35
	s_waitcnt vmcnt(6)
	v_cvt_pk_bf16_f32 v13, v40, v41
	v_cvt_pk_bf16_f32 v12, v38, v39
	ds_write2st64_b64 v239, v[10:11], v[12:13] offset0:32 offset1:40
	s_waitcnt vmcnt(5)
	v_cvt_pk_bf16_f32 v11, v44, v45
	v_cvt_pk_bf16_f32 v10, v42, v43
	s_waitcnt vmcnt(4)
	v_cvt_pk_bf16_f32 v13, v48, v49
	v_cvt_pk_bf16_f32 v12, v46, v47
	ds_write2st64_b64 v239, v[10:11], v[12:13] offset0:48 offset1:56
	s_waitcnt lgkmcnt(0)
	s_add_i32 s21, s21, 2
	s_barrier
	s_waitcnt lgkmcnt(11)
	v_mfma_f32_16x16x32_bf16 v[174:177], v[178:181], v[206:209], v[240:243]
	s_lshl_b32 s22, s21, 1
	s_and_b32 s22, s22, 0x60
	s_add_i32 s22, s22, s12
	s_lshl_b32 s22, s22, 6
	v_mfma_f32_16x16x32_bf16 v[170:173], v[194:197], v[206:209], v[244:247]
	s_and_b32 s22, s22, 0x3f00
	s_or_b32 s22, s22, s13
	s_lshl_b32 s23, s21, 23
	s_lshl_b32 s22, s22, 9
	v_mfma_f32_16x16x32_bf16 v[158:161], v[198:201], v[206:209], v[248:251]
	s_and_b32 s23, s23, 0x7000000
	s_or_b32 s22, s22, s23
	s_lshl_b32 s23, s21, 8
	s_and_b32 s23, s23, 0x100
	s_or_b32 s22, s22, s23
	s_or_b32 s23, s22, 0x4000
	buffer_load_dwordx4 v[10:13], v1, s[4:7], s22 offen sc0 nt
	v_mfma_f32_16x16x32_bf16 v[142:145], v[202:205], v[206:209], v[252:255]
	s_waitcnt lgkmcnt(10)
	v_mfma_f32_16x16x32_bf16 v[166:169], v[178:181], v[210:213], v[240:243]
	v_mfma_f32_16x16x32_bf16 v[162:165], v[194:197], v[210:213], v[244:247]
	v_mfma_f32_16x16x32_bf16 v[146:149], v[198:201], v[210:213], v[248:251]
	buffer_load_dwordx4 v[18:21], v1, s[4:7], s23 offen sc0 nt
	s_or_b32 s23, s22, 0x8000
	v_mfma_f32_16x16x32_bf16 v[122:125], v[202:205], v[210:213], v[252:255]
	s_waitcnt lgkmcnt(9)
	v_mfma_f32_16x16x32_bf16 v[154:157], v[178:181], v[214:217], v[240:243]
	v_mfma_f32_16x16x32_bf16 v[150:153], v[194:197], v[214:217], v[244:247]
	v_mfma_f32_16x16x32_bf16 v[130:133], v[198:201], v[214:217], v[248:251]
	buffer_load_dwordx4 v[22:25], v1, s[4:7], s23 offen sc0 nt
	s_or_b32 s23, s22, 0xc000
	v_mfma_f32_16x16x32_bf16 v[106:109], v[202:205], v[214:217], v[252:255]
	s_waitcnt lgkmcnt(8)
	v_mfma_f32_16x16x32_bf16 v[138:141], v[178:181], v[218:221], v[240:243]
	v_mfma_f32_16x16x32_bf16 v[134:137], v[194:197], v[218:221], v[244:247]
	v_mfma_f32_16x16x32_bf16 v[114:117], v[198:201], v[218:221], v[248:251]
	buffer_load_dwordx4 v[30:33], v1, s[4:7], s23 offen sc0 nt
	s_or_b32 s23, s22, 0x10000
	v_mfma_f32_16x16x32_bf16 v[90:93], v[202:205], v[218:221], v[252:255]
	s_waitcnt lgkmcnt(7)
	v_mfma_f32_16x16x32_bf16 v[126:129], v[178:181], v[222:225], v[240:243]
	v_mfma_f32_16x16x32_bf16 v[118:121], v[194:197], v[222:225], v[244:247]
	v_mfma_f32_16x16x32_bf16 v[98:101], v[198:201], v[222:225], v[248:251]
	buffer_load_dwordx4 v[34:37], v1, s[4:7], s23 offen sc0 nt
	s_or_b32 s23, s22, 0x14000
	v_mfma_f32_16x16x32_bf16 v[74:77], v[202:205], v[222:225], v[252:255]
	s_waitcnt lgkmcnt(6)
	v_mfma_f32_16x16x32_bf16 v[110:113], v[178:181], v[226:229], v[240:243]
	v_mfma_f32_16x16x32_bf16 v[102:105], v[194:197], v[226:229], v[244:247]
	v_mfma_f32_16x16x32_bf16 v[82:85], v[198:201], v[226:229], v[248:251]
	buffer_load_dwordx4 v[38:41], v1, s[4:7], s23 offen sc0 nt
	s_or_b32 s23, s22, 0x18000
	s_or_b32 s22, s22, 0x1c000
	v_mfma_f32_16x16x32_bf16 v[62:65], v[202:205], v[226:229], v[252:255]
	s_waitcnt lgkmcnt(5)
	v_mfma_f32_16x16x32_bf16 v[94:97], v[178:181], v[230:233], v[240:243]
	v_mfma_f32_16x16x32_bf16 v[86:89], v[194:197], v[230:233], v[244:247]
	v_mfma_f32_16x16x32_bf16 v[70:73], v[198:201], v[230:233], v[248:251]
	buffer_load_dwordx4 v[42:45], v1, s[4:7], s23 offen sc0 nt
	v_mfma_f32_16x16x32_bf16 v[54:57], v[202:205], v[230:233], v[252:255]
	s_waitcnt lgkmcnt(4)
	v_mfma_f32_16x16x32_bf16 v[78:81], v[178:181], v[234:237], v[240:243]
	v_mfma_f32_16x16x32_bf16 v[66:69], v[194:197], v[234:237], v[244:247]
	v_mfma_f32_16x16x32_bf16 v[58:61], v[198:201], v[234:237], v[248:251]
	buffer_load_dwordx4 v[46:49], v1, s[4:7], s22 offen sc0 nt
	v_mfma_f32_16x16x32_bf16 v[50:53], v[202:205], v[234:237], v[252:255]
	s_waitcnt lgkmcnt(0)
	s_barrier
	ds_read_b128 v[178:181], v182 offset:33792
	ds_read_b128 v[194:197], v182 offset:35840
	ds_read_b128 v[198:201], v182 offset:37888
	ds_read_b128 v[202:205], v182 offset:39936
	ds_read_b128 v[206:209], v238 offset:1024
	ds_read_b128 v[210:213], v238 offset:3072
	ds_read_b128 v[214:217], v238 offset:5120
	ds_read_b128 v[218:221], v238 offset:7168
	ds_read_b128 v[222:225], v238 offset:9216
	ds_read_b128 v[226:229], v238 offset:11264
	ds_read_b128 v[230:233], v238 offset:13312
	ds_read_b128 v[234:237], v238 offset:15360
	v_add_u32_e32 v182, s19, v190
	s_waitcnt vmcnt(11)
	ds_write_b128 v182, v[2:5] offset:32768
	s_waitcnt vmcnt(10)
	ds_write_b128 v182, v[6:9] offset:40960
	s_waitcnt vmcnt(9)
	ds_write_b128 v182, v[14:17] offset:49152
	s_waitcnt vmcnt(8)
	ds_write_b128 v182, v[26:29] offset:57344
	s_waitcnt lgkmcnt(0)
	s_lshl_b32 s21, s21, 7
	s_and_b32 s21, s21, 0x780
	s_or_b32 s21, s21, s14
	s_or_b32 s22, s21, 0x20000
	buffer_load_dwordx4 v[2:5], v188, s[0:3], s21 offen sc1
	buffer_load_dwordx4 v[6:9], v188, s[0:3], s22 offen sc1
	s_or_b32 s22, s21, 0x40000
	s_or_b32 s21, s21, 0x60000
	buffer_load_dwordx4 v[14:17], v188, s[0:3], s22 offen sc1
	buffer_load_dwordx4 v[26:29], v188, s[0:3], s21 offen sc1
	s_barrier
	s_waitcnt lgkmcnt(11)
	v_mfma_f32_16x16x32_bf16 v[174:177], v[178:181], v[206:209], v[174:177]
	v_mfma_f32_16x16x32_bf16 v[170:173], v[194:197], v[206:209], v[170:173]
	v_mfma_f32_16x16x32_bf16 v[158:161], v[198:201], v[206:209], v[158:161]
	v_mfma_f32_16x16x32_bf16 v[142:145], v[202:205], v[206:209], v[142:145]
	s_waitcnt lgkmcnt(10)
	v_mfma_f32_16x16x32_bf16 v[166:169], v[178:181], v[210:213], v[166:169]
	v_mfma_f32_16x16x32_bf16 v[162:165], v[194:197], v[210:213], v[162:165]
	v_mfma_f32_16x16x32_bf16 v[146:149], v[198:201], v[210:213], v[146:149]
	v_mfma_f32_16x16x32_bf16 v[122:125], v[202:205], v[210:213], v[122:125]
	s_waitcnt lgkmcnt(9)
	v_mfma_f32_16x16x32_bf16 v[154:157], v[178:181], v[214:217], v[154:157]
	v_mfma_f32_16x16x32_bf16 v[150:153], v[194:197], v[214:217], v[150:153]
	v_mfma_f32_16x16x32_bf16 v[130:133], v[198:201], v[214:217], v[130:133]
	v_mfma_f32_16x16x32_bf16 v[106:109], v[202:205], v[214:217], v[106:109]
	s_waitcnt lgkmcnt(8)
	v_mfma_f32_16x16x32_bf16 v[138:141], v[178:181], v[218:221], v[138:141]
	v_mfma_f32_16x16x32_bf16 v[134:137], v[194:197], v[218:221], v[134:137]
	v_mfma_f32_16x16x32_bf16 v[114:117], v[198:201], v[218:221], v[114:117]
	v_mfma_f32_16x16x32_bf16 v[90:93], v[202:205], v[218:221], v[90:93]
	s_waitcnt lgkmcnt(7)
	v_mfma_f32_16x16x32_bf16 v[126:129], v[178:181], v[222:225], v[126:129]
	v_mfma_f32_16x16x32_bf16 v[118:121], v[194:197], v[222:225], v[118:121]
	v_mfma_f32_16x16x32_bf16 v[98:101], v[198:201], v[222:225], v[98:101]
	v_mfma_f32_16x16x32_bf16 v[74:77], v[202:205], v[222:225], v[74:77]
	s_waitcnt lgkmcnt(6)
	v_mfma_f32_16x16x32_bf16 v[110:113], v[178:181], v[226:229], v[110:113]
	v_mfma_f32_16x16x32_bf16 v[102:105], v[194:197], v[226:229], v[102:105]
	v_mfma_f32_16x16x32_bf16 v[82:85], v[198:201], v[226:229], v[82:85]
	v_mfma_f32_16x16x32_bf16 v[62:65], v[202:205], v[226:229], v[62:65]
	s_waitcnt lgkmcnt(5)
	v_mfma_f32_16x16x32_bf16 v[94:97], v[178:181], v[230:233], v[94:97]
	v_mfma_f32_16x16x32_bf16 v[86:89], v[194:197], v[230:233], v[86:89]
	v_mfma_f32_16x16x32_bf16 v[70:73], v[198:201], v[230:233], v[70:73]
	v_mfma_f32_16x16x32_bf16 v[54:57], v[202:205], v[230:233], v[54:57]
	s_waitcnt lgkmcnt(4)
	v_mfma_f32_16x16x32_bf16 v[78:81], v[178:181], v[234:237], v[78:81]
	v_mfma_f32_16x16x32_bf16 v[66:69], v[194:197], v[234:237], v[66:69]
	v_mfma_f32_16x16x32_bf16 v[58:61], v[198:201], v[234:237], v[58:61]
	v_mfma_f32_16x16x32_bf16 v[50:53], v[202:205], v[234:237], v[50:53]
	s_branch .LBB1_3
